# v13 + one static s_setprio 1 for waves 4-7 before the attention queues
# speedup vs baseline: 1.0037x; 1.0028x over previous
.LBB0_6667:
	global_load_dword v11, v[4:5], off
	v_max_f32_e32 v10, v10, v10
	v_add_co_u32_e32 v1, vcc, 64, v1
	s_xor_b64 s[2:3], vcc, -1
	v_max_f32_e32 v2, v2, v2
	s_and_b64 s[2:3], exec, s[2:3]
	v_lshl_add_u64 v[4:5], v[4:5], 0, s[4:5]
	s_or_b64 s[0:1], s[2:3], s[0:1]
	s_waitcnt vmcnt(0)
	v_max_f32_e64 v11, |v11|, |v11|
	v_max_f32_e32 v10, v10, v11
	global_load_dword v11, v[6:7], off
	v_lshl_add_u64 v[6:7], v[6:7], 0, s[4:5]
	s_waitcnt vmcnt(0)
	v_max_f32_e64 v11, |v11|, |v11|
	v_max_f32_e32 v2, v2, v11
	s_andn2_b64 exec, exec, s[0:1]
	s_cbranch_execnz .LBB0_6667
	s_or_b64 exec, exec, s[0:1]
	v_and_b32_e32 v1, 64, v224
	v_add_u32_e32 v4, 64, v1
	v_xor_b32_e32 v1, 32, v224
	v_cmp_lt_i32_e32 vcc, v1, v4
	v_max_f32_e32 v6, v9, v9
	v_max_f32_e32 v7, v8, v8
	v_cndmask_b32_e32 v1, v224, v1, vcc
	v_lshlrev_b32_e32 v1, 2, v1
	ds_bpermute_b32 v5, v1, v9
	s_mov_b32 s0, 0x42c00000
	v_cmp_eq_u32_e64 s[38:39], 0, v197
	s_waitcnt lgkmcnt(0)
	v_max_f32_e32 v5, v5, v5
	v_max_f32_e32 v5, v6, v5
	ds_bpermute_b32 v6, v1, v8
	v_max_f32_e32 v8, v10, v10
	s_waitcnt lgkmcnt(0)
	v_max_f32_e32 v6, v6, v6
	v_max_f32_e32 v6, v7, v6
	ds_bpermute_b32 v7, v1, v10
	ds_bpermute_b32 v1, v1, v2
	v_max_f32_e32 v2, v2, v2
	s_waitcnt lgkmcnt(1)
	v_max_f32_e32 v7, v7, v7
	s_waitcnt lgkmcnt(0)
	v_max_f32_e32 v1, v1, v1
	v_max_f32_e32 v1, v2, v1
	v_xor_b32_e32 v2, 16, v224
	v_cmp_lt_i32_e32 vcc, v2, v4
	v_max_f32_e32 v7, v8, v7
	s_nop 0
	v_cndmask_b32_e32 v2, v224, v2, vcc
	v_lshlrev_b32_e32 v2, 2, v2
	ds_bpermute_b32 v8, v2, v5
	s_waitcnt lgkmcnt(0)
	v_max_f32_e32 v8, v8, v8
	v_max_f32_e32 v5, v5, v8
	ds_bpermute_b32 v8, v2, v6
	s_waitcnt lgkmcnt(0)
	v_max_f32_e32 v8, v8, v8
	v_max_f32_e32 v6, v6, v8
	ds_bpermute_b32 v8, v2, v7
	ds_bpermute_b32 v2, v2, v1
	s_waitcnt lgkmcnt(1)
	v_max_f32_e32 v8, v8, v8
	s_waitcnt lgkmcnt(0)
	v_max_f32_e32 v2, v2, v2
	v_max_f32_e32 v1, v1, v2
	v_xor_b32_e32 v2, 8, v224
	v_cmp_lt_i32_e32 vcc, v2, v4
	v_max_f32_e32 v7, v7, v8
	s_nop 0
	v_cndmask_b32_e32 v2, v224, v2, vcc
	v_lshlrev_b32_e32 v193, 2, v2
	ds_bpermute_b32 v2, v193, v5
	s_waitcnt lgkmcnt(0)
	v_max_f32_e32 v2, v2, v2
	v_max_f32_e32 v2, v5, v2
	ds_bpermute_b32 v5, v193, v6
	s_waitcnt lgkmcnt(0)
	v_max_f32_e32 v5, v5, v5
	v_max_f32_e32 v5, v6, v5
	ds_bpermute_b32 v6, v193, v7
	s_waitcnt lgkmcnt(0)
	v_max_f32_e32 v6, v6, v6
	v_max_f32_e32 v6, v7, v6
	ds_bpermute_b32 v7, v193, v1
	s_waitcnt lgkmcnt(0)
	v_max_f32_e32 v7, v7, v7
	v_max_f32_e32 v1, v1, v7
	v_xor_b32_e32 v7, 4, v224
	v_cmp_lt_i32_e32 vcc, v7, v4
	s_nop 1
	v_cndmask_b32_e32 v7, v224, v7, vcc
	v_lshlrev_b32_e32 v194, 2, v7
	ds_bpermute_b32 v7, v194, v2
	s_waitcnt lgkmcnt(0)
	v_max_f32_e32 v7, v7, v7
	v_max_f32_e32 v2, v2, v7
	ds_bpermute_b32 v7, v194, v5
	s_waitcnt lgkmcnt(0)
	v_max_f32_e32 v7, v7, v7
	v_max_f32_e32 v5, v5, v7
	ds_bpermute_b32 v7, v194, v6
	s_waitcnt lgkmcnt(0)
	v_max_f32_e32 v7, v7, v7
	v_max_f32_e32 v6, v6, v7
	ds_bpermute_b32 v7, v194, v1
	s_waitcnt lgkmcnt(0)
	v_max_f32_e32 v7, v7, v7
	v_max_f32_e32 v7, v1, v7
	v_xor_b32_e32 v1, 2, v224
	v_cmp_lt_i32_e32 vcc, v1, v4
	s_nop 1
	v_cndmask_b32_e32 v1, v224, v1, vcc
	v_lshlrev_b32_e32 v195, 2, v1
	ds_bpermute_b32 v1, v195, v2
	s_waitcnt lgkmcnt(0)
	v_max_f32_e32 v1, v1, v1
	v_max_f32_e32 v2, v2, v1
	ds_bpermute_b32 v1, v195, v5
	s_waitcnt lgkmcnt(0)
	v_max_f32_e32 v1, v1, v1
	v_max_f32_e32 v5, v5, v1
	ds_bpermute_b32 v1, v195, v6
	s_waitcnt lgkmcnt(0)
	v_max_f32_e32 v1, v1, v1
	v_max_f32_e32 v1, v6, v1
	ds_bpermute_b32 v6, v195, v7
	s_waitcnt lgkmcnt(0)
	v_max_f32_e32 v6, v6, v6
	v_max_f32_e32 v199, v7, v6
	v_xor_b32_e32 v6, 1, v224
	v_cmp_lt_i32_e32 vcc, v6, v4
	s_nop 1
	v_cndmask_b32_e32 v4, v224, v6, vcc
	v_lshlrev_b32_e32 v196, 2, v4
	ds_bpermute_b32 v4, v196, v2
	ds_bpermute_b32 v201, v196, v1
	ds_bpermute_b32 v200, v196, v199
	s_waitcnt lgkmcnt(2)
	v_max_f32_e32 v4, v4, v4
	v_max_f32_e32 v2, v2, v4
	ds_bpermute_b32 v4, v196, v5
	v_mul_f32_e32 v2, 0x419fecaf, v2
	s_waitcnt lgkmcnt(0)
	v_max_f32_e32 v4, v4, v4
	v_max_f32_e32 v4, v5, v4
	v_mul_f32_e32 v2, v4, v2
	v_cmp_ngt_f32_e32 vcc, s0, v2
	s_nop 1
	v_cndmask_b32_e64 v2, 0, 1, vcc
	s_nop 0
	v_readfirstlane_b32 s0, v2
	s_bitcmp1_b32 s0, 0
	s_cselect_b64 s[0:1], -1, 0
	s_xor_b64 s[44:45], s[0:1], -1
	v_readfirstlane_b32 s2, v0
	s_nop 3
	s_lshr_b32 s2, s2, 6
	s_cmp_ge_u32 s2, 4
	s_cbranch_scc0 .Lattn_prio_done
	s_setprio 1
.Lattn_prio_done:
	s_add_u32 s28, s60, 0x4000
	s_addc_u32 s29, s61, 0
	s_lshl_b64 s[0:1], s[6:7], 2
	s_add_u32 s46, s28, s0
	s_addc_u32 s47, s29, s1
	s_and_b64 s[2:3], s[36:37], exec
	s_movk_i32 s2, 0x120
	s_cselect_b32 s52, s2, 0x100
	s_add_u32 s53, s60, 0x56190000
	s_addc_u32 s54, s61, 0
	s_add_u32 s55, s60, 0x54690000
	s_addc_u32 s56, s61, 0
	s_branch .LBB0_6672
